# bundle6 + N2 layer-0 path: 16 f32 x chunks loaded in one batch (was 16 serialized load+vmcnt(0) round trips per iteration)
# speedup vs baseline: 1.0241x; 1.0109x over previous
.LBB0_693:
	v_readlane_b32 s22, v254, 12
	s_mov_b32 s6, s22
	s_waitcnt vmcnt(0)
	s_barrier
	v_mbcnt_lo_u32_b32 v0, -1, 0
	v_mbcnt_hi_u32_b32 v0, -1, v0
	v_mbcnt_lo_u32_b32 v222, -1, 0
	v_mbcnt_hi_u32_b32 v222, -1, v222
	s_nop 0
	v_lshl_add_u32 v130, s22, 6, v222
	v_cmp_gt_i32_e64 s[6:7], 32, v130
	v_lshl_add_u32 v230, v130, 2, 0
	s_barrier
	s_and_saveexec_b64 s[8:9], s[6:7]
	v_add_u32_e32 v0, 0x22c00, v230
	ds_write_b32 v0, v65
	s_or_b64 exec, exec, s[8:9]
	v_readlane_b32 s18, v255, 37
	v_readlane_b32 s19, v255, 38
	s_mov_b32 s19, s67
	s_lshl_b64 s[10:11], s[18:19], 3
	s_mul_i32 s9, s18, 0x30000
	v_readlane_b32 s12, v255, 26
	s_mul_hi_u32 s8, s18, 0x30000
	v_readlane_b32 s13, v255, 27
	s_add_u32 s16, s12, s9
	s_addc_u32 s17, s13, s8
	s_mov_b32 s8, s18
	s_add_u32 s14, s16, 0x18000
	v_writelane_b32 v255, s8, 37
	v_readlane_b32 s28, v254, 13
	s_addc_u32 s15, s17, 0
	v_writelane_b32 v255, s9, 38
	s_add_i32 s8, s22, s28
	s_ashr_i32 s9, s8, 8
	s_lshl_b32 s66, s18, 2
	s_ashr_i32 s12, s9, 31
	s_add_u32 s9, s10, s9
	s_addc_u32 s10, s11, s12
	s_mulk_i32 s10, 0x6000
	s_mul_hi_u32 s11, s9, 0x6000
	s_add_i32 s11, s11, s10
	s_mulk_i32 s9, 0x6000
	v_readlane_b32 s12, v255, 28
	v_readlane_b32 s13, v255, 29
	s_add_u32 s9, s12, s9
	s_addc_u32 s23, s13, s11
	v_readlane_b32 s26, v254, 16
	v_readlane_b32 s20, v255, 39
	v_readlane_b32 s27, v254, 17
	s_load_dwordx2 s[18:19], s[26:27], 48
	s_waitcnt lgkmcnt(0)
	v_readlane_b32 s21, v255, 40
	s_add_u32 s20, s18, s20
	s_addc_u32 s21, s19, s21
	v_and_b32_e32 v153, 63, v222
	s_load_dwordx2 s[12:13], s[26:27], 0x98
	s_waitcnt lgkmcnt(0)
	s_add_u32 s18, s9, 0x4000
	s_load_dwordx2 s[10:11], s[26:27], 0xa8
	s_waitcnt lgkmcnt(0)
	s_addc_u32 s19, s23, 0
	v_lshlrev_b32_e32 v152, 4, v153
	global_load_dwordx4 v[60:63], v152, s[18:19]
	v_or_b32_e32 v8, 0x400, v152
	global_load_dwordx4 v[66:69], v8, s[18:19]
	global_load_dwordx4 v[70:73], v152, s[20:21]
	global_load_dwordx4 v[74:77], v152, s[20:21] offset:1024
	global_load_dwordx4 v[142:145], v152, s[20:21] offset:2048
	global_load_dwordx4 v[146:149], v152, s[20:21] offset:3072
	s_add_u32 s20, s9, 0x3000
	s_addc_u32 s21, s23, 0
	s_add_u32 s24, s9, 0x2000
	s_addc_u32 s25, s23, 0
	v_or_b32_e32 v24, 0x800, v152
	v_or_b32_e32 v42, 0xc00, v152
	global_load_dwordx4 v[0:3], v8, s[24:25]
	global_load_dwordx4 v[154:157], v24, s[18:19]
	global_load_dwordx4 v[4:7], v152, s[20:21]
	s_nop 0
	global_load_dwordx4 v[8:11], v8, s[20:21]
	s_nop 0
	global_load_dwordx4 v[158:161], v42, s[18:19]
	global_load_dwordx4 v[12:15], v42, s[20:21]
	v_and_b32_e32 v162, 15, v222
	s_lshl_b32 s9, s22, 7
	v_bfe_u32 v163, v222, 4, 2
	v_lshlrev_b32_e32 v64, 10, v162
	s_ashr_i32 s18, s9, 31
	v_mov_b32_e32 v103, v65
	v_or_b32_e32 v102, 0x4000, v64
	v_lshl_or_b32 v120, v163, 3, s9
	v_mov_b32_e32 v121, s18
	v_mov_b32_e32 v119, v65
	v_or_b32_e32 v118, 0x8000, v64
	v_or_b32_e32 v28, 32, v120
	v_lshl_add_u64 v[32:33], v[120:121], 0, v[102:103]
	v_mov_b32_e32 v29, s18
	v_lshl_add_u64 v[30:31], v[120:121], 0, v[64:65]
	v_lshl_add_u64 v[34:35], v[120:121], 0, v[118:119]
	v_lshlrev_b64 v[32:33], 1, v[32:33]
	v_lshl_add_u64 v[36:37], v[28:29], 0, v[64:65]
	v_lshl_add_u64 v[38:39], v[28:29], 0, v[102:103]
	v_lshlrev_b64 v[30:31], 1, v[30:31]
	v_lshlrev_b64 v[34:35], 1, v[34:35]
	v_lshl_add_u64 v[28:29], v[28:29], 0, v[118:119]
	v_lshl_add_u64 v[40:41], s[14:15], 0, v[32:33]
	v_lshl_add_u64 v[52:53], v[36:37], 1, s[14:15]
	v_lshl_add_u64 v[56:57], v[38:39], 1, s[14:15]
	global_load_dwordx4 v[16:19], v152, s[24:25]
	global_load_dwordx4 v[20:23], v24, s[20:21]
	s_nop 0
	global_load_dwordx4 v[24:27], v24, s[24:25]
	v_lshl_add_u64 v[98:99], s[16:17], 0, v[30:31]
	v_lshl_add_u64 v[94:95], s[14:15], 0, v[30:31]
	v_lshl_add_u64 v[106:107], s[16:17], 0, v[32:33]
	v_lshl_add_u64 v[122:123], s[16:17], 0, v[34:35]
	v_lshl_add_u64 v[124:125], s[14:15], 0, v[34:35]
	v_lshl_add_u64 v[80:81], v[28:29], 1, s[14:15]
	global_load_dwordx4 v[28:31], v42, s[24:25]
	global_load_dwordx4 v[32:35], v[98:99], off
	global_load_dwordx4 v[36:39], v[40:41], off
	s_nop 0
	global_load_dwordx4 v[40:43], v[122:123], off
	global_load_dwordx4 v[44:47], v[106:107], off
	global_load_dwordx4 v[48:51], v[106:107], off offset:64
	s_nop 0
	global_load_dwordx4 v[52:55], v[52:53], off
	s_nop 0
	global_load_dwordx4 v[56:59], v[56:57], off
	v_or_b32_e32 v78, 64, v120
	v_mov_b32_e32 v79, s18
	v_or_b32_e32 v120, 0x60, v120
	v_lshl_add_u64 v[88:89], v[78:79], 0, v[118:119]
	v_lshl_add_u64 v[104:105], v[120:121], 0, v[64:65]
	v_lshl_add_u64 v[112:113], v[120:121], 0, v[102:103]
	v_lshl_add_u64 v[126:127], v[120:121], 0, v[118:119]
	v_lshl_add_u64 v[90:91], v[88:89], 1, s[14:15]
	v_lshl_add_u64 v[110:111], v[104:105], 1, s[14:15]
	v_lshl_add_u64 v[114:115], v[112:113], 1, s[14:15]
	v_lshl_add_u64 v[126:127], v[126:127], 1, s[14:15]
	s_lshl_b32 s16, s22, 8
	s_ashr_i32 s9, s8, 31
	v_readlane_b32 s21, v255, 7
	s_movk_i32 s20, 0xc0
	v_lshlrev_b32_e32 v131, 3, v153
	v_add_u32_e32 v236, s61, v131
	s_waitcnt vmcnt(22)
	v_pk_add_f32 v[60:61], v[60:61], 1.0 op_sel_hi:[1,0]
	s_waitcnt vmcnt(21)
	v_pk_add_f32 v[66:67], v[66:67], 1.0 op_sel_hi:[1,0]
	s_waitcnt vmcnt(20)
	v_pk_mul_f32 v[134:135], v[70:71], v[60:61]
	v_lshl_add_u64 v[70:71], v[78:79], 0, v[64:65]
	v_pk_add_f32 v[62:63], v[62:63], 1.0 op_sel_hi:[1,0]
	v_pk_add_f32 v[68:69], v[68:69], 1.0 op_sel_hi:[1,0]
	s_waitcnt vmcnt(19)
	v_pk_mul_f32 v[138:139], v[74:75], v[66:67]
	v_lshl_add_u64 v[74:75], v[70:71], 1, s[14:15]
	v_pk_mul_f32 v[132:133], v[72:73], v[62:63]
	v_pk_mul_f32 v[136:137], v[76:77], v[68:69]
	global_load_dwordx4 v[60:63], v[98:99], off offset:64
	global_load_dwordx4 v[66:69], v[98:99], off offset:128
	global_load_dwordx4 v[70:73], v[80:81], off
	s_nop 0
	global_load_dwordx4 v[74:77], v[74:75], off
	v_lshl_add_u64 v[80:81], v[78:79], 0, v[102:103]
	v_lshl_add_u64 v[86:87], v[80:81], 1, s[14:15]
	global_load_dwordx4 v[78:81], v[122:123], off offset:64
	global_load_dwordx4 v[82:85], v[122:123], off offset:128
	s_nop 0
	global_load_dwordx4 v[86:89], v[86:87], off
	s_nop 0
	global_load_dwordx4 v[90:93], v[90:91], off
	s_nop 0
	global_load_dwordx4 v[94:97], v[94:95], off
	s_nop 0
	global_load_dwordx4 v[98:101], v[98:99], off offset:192
	s_nop 0
	global_load_dwordx4 v[102:105], v[106:107], off offset:128
	s_nop 0
	global_load_dwordx4 v[106:109], v[106:107], off offset:192
	s_nop 0
	global_load_dwordx4 v[110:113], v[110:111], off
	s_nop 0
	global_load_dwordx4 v[114:117], v[114:115], off
	s_nop 0
	global_load_dwordx4 v[118:121], v[124:125], off
	s_nop 0
	global_load_dwordx4 v[122:125], v[122:123], off offset:192
	s_waitcnt vmcnt(31)
	v_pk_add_f32 v[140:141], v[156:157], 1.0 op_sel_hi:[1,0]
	global_load_dwordx4 v[126:129], v[126:127], off
	v_pk_mul_f32 v[140:141], v[144:145], v[140:141]
	s_waitcnt vmcnt(29)
	v_pk_add_f32 v[144:145], v[160:161], 1.0 op_sel_hi:[1,0]
	v_pk_add_f32 v[150:151], v[154:155], 1.0 op_sel_hi:[1,0]
	v_pk_mul_f32 v[144:145], v[148:149], v[144:145]
	v_and_or_b32 v148, v222, 48, s16
	s_lshl_b32 s16, s22, 5
	v_lshl_or_b32 v149, v163, 2, s16
	s_lshl_b64 s[16:17], s[66:67], 2
	s_add_u32 s16, s12, s16
	s_addc_u32 s17, s13, s17
	v_readlane_b32 s12, v255, 41
	v_pk_mul_f32 v[142:143], v[142:143], v[150:151]
	v_pk_add_f32 v[150:151], v[158:159], 1.0 op_sel_hi:[1,0]
	v_readlane_b32 s13, v255, 42
	s_add_u32 s18, s10, s12
	v_pk_mul_f32 v[146:147], v[146:147], v[150:151]
	s_addc_u32 s19, s11, s13
	s_movk_i32 s11, 0x810
	v_mov_b32_e32 v151, 0x8100
	v_mad_u32_u24 v151, v162, s11, v151
	v_or_b32_e32 v154, 64, v148
	v_mad_u32_u24 v232, v162, s11, v148
	v_add_u32_e32 v233, v151, v148
	v_mad_u32_u24 v157, v162, s11, v154
	v_add_u32_e32 v158, v154, v151
	v_or_b32_e32 v154, 0x80, v148
	v_or_b32_e32 v148, 0xc0, v148
	v_lshl_add_u32 v156, v162, 2, 0
	v_mad_u32_u24 v159, v162, s11, v154
	v_mad_u32_u24 v161, v162, s11, v148
	v_add_u32_e32 v162, v148, v151
	v_lshlrev_b32_e32 v148, 2, v130
	v_add_u32_e32 v234, 0, v148
	v_add_u32_e32 v235, s21, v148
	v_lshlrev_b32_e32 v148, 3, v222
	v_mul_lo_u32 v64, v130, s20
	v_ashrrev_i32_e32 v150, 2, v130
	s_mul_i32 s10, s22, 0x2040
	v_add_u32_e32 v160, v154, v151
	v_and_b32_e32 v151, 24, v148
	s_load_dwordx2 s[14:15], s[26:27], 0
	s_waitcnt lgkmcnt(0)
	v_add_u32_e32 v231, s21, v64
	v_add_u32_e32 v64, s28, v150
	s_add_i32 s24, s10, 0x810
	s_add_i32 s25, s10, 0x1020
	s_add_i32 s26, s10, 0x1830
	s_add_i32 s27, s10, 0
	s_add_i32 s28, s61, s10
	v_lshl_or_b32 v148, v150, 8, v151
	v_readlane_b32 s10, v255, 8
	v_mul_lo_u32 v163, v149, s20
	s_add_i32 s29, s61, s24
	v_add_u32_e32 v237, s10, v148
	v_lshlrev_b64 v[148:149], 8, v[64:65]
	v_or_b32_e32 v148, v148, v151
	s_mov_b64 s[10:11], 0x300000
	v_lshl_add_u64 v[148:149], v[148:149], 0, s[10:11]
	s_lshl_b64 s[10:11], s[8:9], 15
	s_add_i32 s30, s61, s25
	s_add_i32 s31, s61, s26
	v_lshl_or_b32 v150, v153, 2, s10
	v_mov_b32_e32 v151, s11
	s_lshl_b64 s[10:11], s[8:9], 17
	s_add_u32 s10, s14, s10
	v_mov_b32_e32 v153, v65
	s_addc_u32 s11, s15, s11
	s_lshl_b64 s[8:9], s[8:9], 16
	v_lshl_add_u64 v[152:153], s[10:11], 0, v[152:153]
	v_or_b32_e32 v154, s8, v131
	v_mov_b32_e32 v155, s9
	s_mov_b64 s[20:21], 0
	v_add_u32_e32 v238, v156, v163
	v_add_u32_e32 v239, s61, v157
	v_add_u32_e32 v240, s61, v158
	v_add_u32_e32 v241, s61, v159
	v_add_u32_e32 v242, s61, v160
	v_add_u32_e32 v243, s61, v161
	v_add_u32_e32 v244, s61, v162
	v_mbcnt_lo_u32_b32 v200, -1, 0
	v_mbcnt_hi_u32_b32 v200, -1, v200
	v_lshlrev_b32_e32 v201, 2, v200
	v_cmp_gt_u32_e32 vcc, 4, v200
	s_and_saveexec_b64 s[8:9], vcc
	global_load_dword v202, v201, s[16:17]
	s_or_b64 exec, exec, s[8:9]
	v_cmp_gt_u32_e32 vcc, 32, v200
	s_and_saveexec_b64 s[8:9], vcc
	global_load_dword v203, v201, s[18:19]
	s_or_b64 exec, exec, s[8:9]
	s_waitcnt vmcnt(0)
	v_add_u32_e32 v204, 0x24000, v201
	v_cmp_gt_u32_e32 vcc, 4, v200
	s_and_saveexec_b64 s[8:9], vcc
	ds_write_b32 v204, v202
	s_or_b64 exec, exec, s[8:9]
	v_cmp_gt_u32_e32 vcc, 32, v200
	s_and_saveexec_b64 s[8:9], vcc
	ds_write_b32 v204, v203 offset:16
	s_or_b64 exec, exec, s[8:9]
	s_waitcnt lgkmcnt(0)
	s_mov_b64 s[98:99], 0x1000
	s_add_u32 s100, s42, 0x6800000
	s_addc_u32 s101, s43, 0
	s_branch .LBB0_697

.Ln2l0_top:
	v_lshl_add_u64 v[172:173], v[152:153], 0, s[20:21]
	v_lshl_add_u64 v[250:251], v[172:173], 0, s[98:99]
	v_lshl_add_u64 v[252:253], v[172:173], 0, s[46:47]
	v_lshl_add_u64 v[220:221], v[252:253], 0, s[98:99]
	global_load_dwordx4 v[174:177], v[172:173], off nt
	global_load_dwordx4 v[206:209], v[172:173], off offset:1024 nt
	global_load_dwordx4 v[210:213], v[172:173], off offset:2048 nt
	global_load_dwordx4 v[214:217], v[172:173], off offset:3072 nt
	global_load_dwordx4 v[190:193], v[250:251], off nt
	global_load_dwordx4 v[194:197], v[250:251], off offset:1024 nt
	global_load_dwordx4 v[198:201], v[250:251], off offset:2048 nt
	global_load_dwordx4 v[202:205], v[250:251], off offset:3072 nt
	global_load_dwordx4 v[246:249], v[252:253], off nt
	global_load_dwordx4 v[178:181], v[252:253], off offset:1024 nt
	global_load_dwordx4 v[182:185], v[252:253], off offset:2048 nt
	global_load_dwordx4 v[186:189], v[252:253], off offset:3072 nt
	global_load_dwordx4 v[156:159], v[220:221], off nt
	global_load_dwordx4 v[224:227], v[220:221], off offset:1024 nt
	global_load_dwordx4 v[160:163], v[220:221], off offset:2048 nt
	global_load_dwordx4 v[166:169], v[220:221], off offset:3072 nt
	s_waitcnt vmcnt(0)
	v_cvt_pk_f16_f32 v174, v174, v175
	v_cvt_pk_f16_f32 v175, v176, v177
	v_cvt_pk_f16_f32 v209, v208, v209
	v_cvt_pk_f16_f32 v208, v206, v207
	v_cvt_pk_f16_f32 v210, v210, v211
	v_cvt_pk_f16_f32 v211, v212, v213
	v_cvt_pk_f16_f32 v217, v216, v217
	v_cvt_pk_f16_f32 v216, v214, v215
	v_cvt_pk_f16_f32 v193, v192, v193
	v_cvt_pk_f16_f32 v192, v190, v191
	v_cvt_pk_f16_f32 v194, v194, v195
	v_cvt_pk_f16_f32 v195, v196, v197
	v_cvt_pk_f16_f32 v198, v198, v199
	v_cvt_pk_f16_f32 v199, v200, v201
	v_cvt_pk_f16_f32 v202, v202, v203
	v_cvt_pk_f16_f32 v203, v204, v205
	v_cvt_pk_f16_f32 v176, v246, v247
	v_cvt_pk_f16_f32 v177, v248, v249
	v_cvt_pk_f16_f32 v178, v178, v179
	v_cvt_pk_f16_f32 v179, v180, v181
	v_cvt_pk_f16_f32 v182, v182, v183
	v_cvt_pk_f16_f32 v183, v184, v185
	v_cvt_pk_f16_f32 v186, v186, v187
	v_cvt_pk_f16_f32 v187, v188, v189
	v_cvt_pk_f16_f32 v156, v156, v157
	v_cvt_pk_f16_f32 v157, v158, v159
	v_cvt_pk_f16_f32 v158, v224, v225
	v_cvt_pk_f16_f32 v159, v226, v227
	v_cvt_pk_f16_f32 v163, v162, v163
	v_cvt_pk_f16_f32 v162, v160, v161
	v_cvt_pk_f16_f32 v169, v168, v169
	v_cvt_pk_f16_f32 v168, v166, v167
	v_add_u32_e32 v245, 0x1000, v154
	global_load_dwordx2 v[212:213], v154, s[100:101]
	global_load_dwordx2 v[214:215], v154, s[100:101] offset:512
	global_load_dwordx2 v[218:219], v154, s[100:101] offset:1024
	global_load_dwordx2 v[220:221], v154, s[100:101] offset:1536
	global_load_dwordx2 v[196:197], v154, s[100:101] offset:2048
	global_load_dwordx2 v[200:201], v154, s[100:101] offset:2560
	global_load_dwordx2 v[204:205], v154, s[100:101] offset:3072
	global_load_dwordx2 v[206:207], v154, s[100:101] offset:3584
	global_load_dwordx2 v[180:181], v245, s[100:101]
	global_load_dwordx2 v[184:185], v245, s[100:101] offset:512
	global_load_dwordx2 v[188:189], v245, s[100:101] offset:1024
	global_load_dwordx2 v[190:191], v245, s[100:101] offset:1536
	global_load_dwordx2 v[160:161], v245, s[100:101] offset:2048
	global_load_dwordx2 v[166:167], v245, s[100:101] offset:2560
	global_load_dwordx2 v[170:171], v245, s[100:101] offset:3072
	s_waitcnt vmcnt(0)
	s_branch .LBB0_745
